# baseline (speedup 1.0000x reference)
.LBB2_13:
	s_waitcnt vmcnt(0)
	s_barrier
	s_add_i32 s16, s22, 0xffffc000
	s_and_b32 s16, s16, 0xc000
	v_add_u32_e32 v34, s16, v108
	s_add_u32 s16, s12, 0xfffce000
	s_addc_u32 s17, s13, -1
	v_readfirstlane_b32 s26, v34
	v_lshl_add_u64 v[34:35], s[16:17], 0, v[84:85]
	s_mov_b32 s27, m0
	s_mov_b32 m0, s26
	s_nop 0
	global_load_lds_dwordx4 v[34:35], off
	s_mov_b32 m0, s27
	v_lshl_add_u64 v[34:35], s[16:17], 0, v[86:87]
	s_add_i32 s16, s26, 0x400
	s_mov_b32 s17, m0
	s_mov_b32 m0, s16
	s_nop 0
	global_load_lds_dwordx4 v[34:35], off
	s_mov_b32 m0, s17
	s_and_b32 s16, s22, 0xc000
	v_add_u32_e32 v34, s16, v108
	s_nop 0
	v_readfirstlane_b32 s16, v34
	v_lshl_add_u64 v[34:35], s[12:13], 0, v[84:85]
	s_mov_b32 s17, m0
	s_mov_b32 m0, s16
	s_nop 0
	global_load_lds_dwordx4 v[34:35], off
	s_mov_b32 m0, s17
	v_lshl_add_u64 v[34:35], s[12:13], 0, v[86:87]
	s_addk_i32 s16, 0x400
	s_mov_b32 s17, m0
	s_mov_b32 m0, s16
	s_nop 0
	global_load_lds_dwordx4 v[34:35], off
	s_mov_b32 m0, s17
	v_add_u32_e32 v34, s22, v109
	v_add_u32_e32 v34, 0xffff4000, v34
	v_and_b32_e32 v34, 0xc000, v34
	v_add_u32_e32 v114, 0, v34
	v_add_u32_e32 v38, v114, v106
	v_add_u32_e32 v82, v114, v105
	ds_read_b128 v[34:37], v38
	ds_read_b128 v[38:41], v38 offset:4096
	ds_read_b128 v[116:119], v82
	ds_read_b128 v[120:123], v82 offset:4096
	v_add_u32_e32 v82, v114, v104
	s_waitcnt lgkmcnt(2)
	v_mfma_f32_32x32x16_f16 v[50:65], v[34:37], v[78:81], 0
	v_mfma_f32_32x32x16_f16 v[34:49], v[38:41], v[78:81], 0
	s_waitcnt lgkmcnt(1)
	v_mfma_f32_32x32x16_f16 v[50:65], v[116:119], v[74:77], v[50:65]
	s_waitcnt lgkmcnt(0)
	v_mfma_f32_32x32x16_f16 v[34:49], v[120:123], v[74:77], v[34:49]
	ds_read_b128 v[116:119], v82
	ds_read_b128 v[120:123], v82 offset:4096
	v_add_u32_e32 v82, v114, v103
	s_waitcnt lgkmcnt(1)
	v_mfma_f32_32x32x16_f16 v[50:65], v[116:119], v[70:73], v[50:65]
	s_waitcnt lgkmcnt(0)
	v_mfma_f32_32x32x16_f16 v[34:49], v[120:123], v[70:73], v[34:49]
	ds_read_b128 v[116:119], v82
	ds_read_b128 v[120:123], v82 offset:4096
	s_waitcnt lgkmcnt(1)
	v_mfma_f32_32x32x16_f16 v[50:65], v[116:119], v[66:69], v[50:65]
	s_waitcnt lgkmcnt(0)
	v_mfma_f32_32x32x16_f16 v[34:49], v[120:123], v[66:69], v[34:49]
	s_nop 9
	v_max3_f32 v82, v50, v51, v52
	v_max3_f32 v82, v82, v53, v54
	v_max3_f32 v82, v82, v55, v56
	v_max3_f32 v82, v82, v57, v58
	v_max3_f32 v82, v82, v59, v60
	v_max3_f32 v82, v82, v61, v62
	v_max_f32_e32 v91, v65, v65
	v_max3_f32 v89, v34, v35, v36
	v_max3_f32 v89, v89, v37, v38
	v_max3_f32 v89, v89, v39, v40
	v_max3_f32 v89, v89, v41, v42
	v_max3_f32 v89, v89, v43, v44
	v_max3_f32 v89, v89, v45, v46
	v_max_f32_e32 v90, v49, v49
	v_max3_f32 v82, v82, v63, v64
	v_max3_f32 v89, v89, v47, v48
	v_max_f32_e32 v90, v91, v90
	v_max3_f32 v82, v82, v89, v90
	v_mov_b32_e32 v89, v82
	s_nop 1
	v_permlane32_swap_b32_e32 v82, v89
	v_max_f32_e32 v82, v82, v89
	v_fma_f32 v89, v82, s23, -v88
	v_cmp_lt_f32_e32 vcc, s24, v89
	s_cbranch_vccz .LBB2_16
	v_mul_f32_e32 v82, 0x3e38aa3b, v82
	v_max_f32_e32 v82, v82, v82
	v_max_f32_e32 v89, v88, v88
	v_max_f32_e32 v102, v89, v82
	v_sub_f32_e32 v82, v88, v102
	v_exp_f32_e32 v82, v82
	s_and_saveexec_b64 s[16:17], s[4:5]
	s_cbranch_execz .LBB2_11
	v_lshl_add_u32 v88, v95, 2, v100
	ds_write_b32 v88, v82
	s_branch .LBB2_11
